# best5 + DIL unit order remap for L2 locality + removed redundant duplicate logits pass in WIN1 + rewritten logits (16-col) pass: all 256 WGs, K-split across wave pairs, 32 loads in flight
# speedup vs baseline: 1.0263x; 1.0073x over previous
.LBB0_474:
	s_and_b32 s3, s96, 7
	s_mulk_i32 s3, 0x180
	s_ashr_i32 s6, s96, 3
	s_add_i32 s9, s3, s6
	s_and_b64 s[6:7], s[0:1], exec
	s_cselect_b32 s48, s9, s96
	s_addk_i32 s3, 0x180
	s_and_b64 s[6:7], s[0:1], exec
	s_cselect_b32 s3, s3, 0xc00
	s_cmp_ge_i32 s48, s3
	s_waitcnt vmcnt(0)
	s_barrier
	s_cbranch_scc1 .LBB0_479
	s_ashr_i32 s6, s2, 31
	s_lshr_b32 s6, s6, 29
	s_add_i32 s6, s2, s6
	s_ashr_i32 s6, s6, 3
	s_and_b64 s[0:1], s[0:1], exec
	s_cselect_b32 s33, s6, s2
	s_add_u32 s36, s58, 0x41a00000
	s_addc_u32 s37, s59, 0
	s_add_u32 s38, s58, 0x4da00000
	s_addc_u32 s39, s59, 0
	s_add_u32 s40, s58, 0x53a00000
	s_addc_u32 s41, s59, 0
	s_mov_b32 s100, s48
	s_lshr_b32 s0, s100, 6
	s_mul_i32 s0, s0, 43
	s_lshr_b32 s0, s0, 7
	s_mul_i32 s1, s0, 0xc0
	s_sub_i32 s1, s100, s1
	s_lshr_b32 s6, s1, 4
	s_mul_i32 s6, s6, 43
	s_lshr_b32 s6, s6, 7
	s_mul_i32 s9, s6, 48
	s_sub_i32 s1, s1, s9
	s_lshr_b32 s9, s1, 4
	s_and_b32 s1, s1, 15
	s_lshl_b32 s9, s9, 1
	s_sub_i32 s48, 4, s9
	s_lshr_b32 s10, s1, s48
	s_lshl_b32 s6, s6, s48
	s_lshl_b32 s48, s10, s48
	s_sub_i32 s1, s1, s48
	s_or_b32 s1, s1, s6
	s_lshl_b32 s48, s48, 2
	s_or_b32 s48, s48, s1
	s_lshl_b32 s0, s0, 6
	s_or_b32 s48, s48, s0
	s_lshl_b32 s9, s9, 9
	s_or_b32 s48, s48, s9
	s_ashr_i32 s1, s48, 9
	s_and_b32 s9, s1, -2
	s_and_b32 s0, s48, 63
	s_sub_i32 s1, 6, s9
	s_lshr_b32 s10, s0, s1
	s_lshr_b32 s1, 64, s9
	s_add_i32 s1, s1, -1
	s_and_b32 s0, s1, s0
	s_lshl_b32 s11, s0, 7
	s_lshl_b32 s0, s48, 4
	s_and_b32 s0, s0, 0x2000
	s_mulk_i32 s0, 0x3000
	v_lshrrev_b32_e32 v83, 4, v0
	s_add_u32 s0, s36, s0
	s_addc_u32 s1, s37, 0
	s_lshl_b32 s6, s48, 2
	v_or_b32_e32 v133, 0xffffff80, v83
	s_and_b32 s6, s6, 0x700
	v_add_u32_e32 v36, s11, v133
	v_and_b32_e32 v1, 15, v0
	s_add_u32 s6, s0, s6
	v_max_i32_e32 v2, 0, v36
	s_addc_u32 s7, s1, 0
	v_mov_b32_e32 v131, 0
	v_lshlrev_b32_e32 v130, 4, v1
	v_lshlrev_b32_e32 v2, s9, v2
	s_movk_i32 s47, 0x3000
	v_lshl_add_u64 v[34:35], s[6:7], 0, v[130:131]
	v_add_u32_e32 v2, s10, v2
	v_max_i32_e32 v10, 0xffffffe0, v36
	s_movk_i32 s46, 0x2000
	v_mad_u64_u32 v[2:3], s[0:1], v2, s47, v[34:35]
	v_add_lshl_u32 v10, v10, 32, s9
	v_or_b32_e32 v18, 64, v36
	v_add_co_u32_e32 v6, vcc, s46, v2
	v_add_u32_e32 v10, s10, v10
	v_max_i32_e32 v18, 0, v18
	v_addc_co_u32_e32 v7, vcc, 0, v3, vcc
	v_mad_u64_u32 v[10:11], s[0:1], v10, s47, v[34:35]
	v_lshlrev_b32_e32 v18, s9, v18
	v_max_i32_e32 v26, 0xffffffa0, v36
	v_add_co_u32_e32 v14, vcc, s46, v10
	v_add_u32_e32 v18, s10, v18
	v_add_u32_e32 v26, 0x60, v26
	v_addc_co_u32_e32 v15, vcc, 0, v11, vcc
	v_mad_u64_u32 v[18:19], s[0:1], v18, s47, v[34:35]
	v_lshlrev_b32_e32 v26, s9, v26
	v_add_co_u32_e32 v22, vcc, s46, v18
	v_add_u32_e32 v26, s10, v26
	s_nop 0
	v_addc_co_u32_e32 v23, vcc, 0, v19, vcc
	v_mad_u64_u32 v[26:27], s[0:1], v26, s47, v[34:35]
	global_load_dwordx4 v[2:5], v[6:7], off
	s_nop 0
	global_load_dwordx4 v[6:9], v[6:7], off offset:2048
	s_nop 0
	global_load_dwordx4 v[10:13], v[14:15], off
	s_nop 0
	global_load_dwordx4 v[14:17], v[14:15], off offset:2048
	s_nop 0
	global_load_dwordx4 v[18:21], v[22:23], off
	s_nop 0
	global_load_dwordx4 v[22:25], v[22:23], off offset:2048
	v_add_co_u32_e32 v30, vcc, s46, v26
	s_movk_i32 s49, 0xffe0
	s_nop 0
	v_addc_co_u32_e32 v31, vcc, 0, v27, vcc
	global_load_dwordx4 v[26:29], v[30:31], off
	s_nop 0
	global_load_dwordx4 v[30:33], v[30:31], off offset:2048
	v_cmp_gt_i32_e32 vcc, 0, v36
	s_movk_i32 s50, 0xffa0
	v_cmp_gt_i32_e64 s[0:1], s49, v36
	v_bfe_u32 v85, v0, 4, 2
	v_lshlrev_b32_e32 v86, 4, v85
	v_mov_b32_e32 v87, v131
	s_mov_b64 s[28:29], 0x1800
	s_movk_i32 s60, 0x1000
	v_lshlrev_b32_e32 v132, 2, v85
	v_or_b32_e32 v101, 1, v132
	v_or_b32_e32 v89, 0x80, v1
	v_bfe_u32 v90, v0, 2, 2
	v_lshlrev_b32_e32 v82, 3, v1
	v_lshlrev_b32_e32 v91, 3, v0
	s_movk_i32 s26, 0x120
	v_lshlrev_b32_e32 v84, 3, v85
	v_and_b32_e32 v91, 24, v91
	v_or_b32_e32 v137, 2, v132
	v_or_b32_e32 v138, 3, v132
	s_mov_b32 s27, 0
	v_cmp_ge_u32_e64 s[12:13], v137, v1
	v_cmp_ge_u32_e64 s[14:15], v138, v1
	v_or_b32_e32 v139, 16, v132
	v_or_b32_e32 v140, 17, v132
	v_or_b32_e32 v141, 18, v132
	v_or_b32_e32 v142, 19, v132
	v_or_b32_e32 v143, 32, v132
	v_or_b32_e32 v144, 33, v132
	v_or_b32_e32 v145, 34, v132
	v_or_b32_e32 v146, 35, v132
	v_or_b32_e32 v147, 48, v132
	v_or_b32_e32 v148, 49, v132
	v_or_b32_e32 v149, 50, v132
	v_or_b32_e32 v150, 51, v132
	v_or_b32_e32 v151, 64, v132
	v_or_b32_e32 v152, 0x41, v132
	v_or_b32_e32 v153, 0x42, v132
	v_or_b32_e32 v154, 0x43, v132
	v_or_b32_e32 v155, 0x50, v132
	v_or_b32_e32 v156, 0x51, v132
	v_or_b32_e32 v157, 0x52, v132
	v_or_b32_e32 v158, 0x53, v132
	v_or_b32_e32 v159, 0x60, v132
	v_or_b32_e32 v160, 0x61, v132
	v_or_b32_e32 v161, 0x62, v132
	v_or_b32_e32 v162, 0x63, v132
	v_or_b32_e32 v163, 0x70, v132
	v_or_b32_e32 v164, 0x71, v132
	v_or_b32_e32 v165, 0x72, v132
	v_or_b32_e32 v166, 0x73, v132
	v_cmp_gt_u32_e64 s[16:17], v132, v1
	v_lshlrev_b32_e32 v134, 1, v84
	v_mov_b32_e32 v180, 0xf149f2ca
	v_mov_b32_e32 v181, 0x41b17218
	s_waitcnt vmcnt(7)
	v_cndmask_b32_e64 v81, v5, 0, vcc
	v_cndmask_b32_e64 v80, v4, 0, vcc
	v_cndmask_b32_e64 v79, v3, 0, vcc
	v_cndmask_b32_e64 v78, v2, 0, vcc
	s_waitcnt vmcnt(6)
	v_cndmask_b32_e64 v73, v9, 0, vcc
	v_cndmask_b32_e64 v72, v8, 0, vcc
	v_cndmask_b32_e64 v71, v7, 0, vcc
	v_cndmask_b32_e64 v70, v6, 0, vcc
	s_waitcnt vmcnt(3)
	v_cndmask_b32_e64 v69, v21, 0, vcc
	v_cndmask_b32_e64 v68, v20, 0, vcc
	v_cndmask_b32_e64 v67, v19, 0, vcc
	v_cndmask_b32_e64 v66, v18, 0, vcc
	s_waitcnt vmcnt(2)
	v_cndmask_b32_e64 v57, v25, 0, vcc
	v_cndmask_b32_e64 v56, v24, 0, vcc
	v_cndmask_b32_e64 v55, v23, 0, vcc
	v_cndmask_b32_e64 v54, v22, 0, vcc
	v_cmp_gt_i32_e32 vcc, s50, v36
	v_cndmask_b32_e64 v74, v10, 0, s[0:1]
	v_add_u32_e32 v2, 0x80, v36
	s_waitcnt vmcnt(1)
	v_cndmask_b32_e64 v58, v26, 0, vcc
	v_add_u32_e32 v10, 0xa0, v36
	v_add_u32_e32 v18, 0xc0, v36
	v_add_u32_e32 v26, 0xe0, v36
	v_lshlrev_b32_e32 v2, s9, v2
	v_lshlrev_b32_e32 v10, s9, v10
	v_lshlrev_b32_e32 v18, s9, v18
	v_lshlrev_b32_e32 v26, s9, v26
	v_add_u32_e32 v2, s10, v2
	v_add_u32_e32 v10, s10, v10
	v_add_u32_e32 v18, s10, v18
	v_add_u32_e32 v26, s10, v26
	v_cndmask_b32_e64 v77, v13, 0, s[0:1]
	v_cndmask_b32_e64 v76, v12, 0, s[0:1]
	v_cndmask_b32_e64 v75, v11, 0, s[0:1]
	v_cndmask_b32_e64 v65, v17, 0, s[0:1]
	v_cndmask_b32_e64 v64, v16, 0, s[0:1]
	v_cndmask_b32_e64 v63, v15, 0, s[0:1]
	v_cndmask_b32_e64 v62, v14, 0, s[0:1]
	v_cndmask_b32_e64 v59, v27, 0, vcc
	v_mad_u64_u32 v[2:3], s[0:1], v2, s47, v[34:35]
	v_mad_u64_u32 v[10:11], s[0:1], v10, s47, v[34:35]
	v_mad_u64_u32 v[18:19], s[0:1], v18, s47, v[34:35]
	v_mad_u64_u32 v[26:27], s[0:1], v26, s47, v[34:35]
	v_cndmask_b32_e64 v61, v29, 0, vcc
	v_cndmask_b32_e64 v60, v28, 0, vcc
	s_waitcnt vmcnt(0)
	v_cndmask_b32_e64 v53, v33, 0, vcc
	v_cndmask_b32_e64 v52, v32, 0, vcc
	v_cndmask_b32_e64 v51, v31, 0, vcc
	v_cndmask_b32_e64 v50, v30, 0, vcc
	v_add_co_u32_e32 v6, vcc, s46, v2
	s_lshr_b32 s0, s8, 2
	s_nop 0
	v_addc_co_u32_e32 v7, vcc, 0, v3, vcc
	s_and_b32 s51, s0, 0x3ffffff0
	v_add_co_u32_e32 v14, vcc, s46, v10
	s_add_i32 s11, s11, s51
	s_nop 0
	v_addc_co_u32_e32 v15, vcc, 0, v11, vcc
	v_or_b32_e32 v34, s11, v1
	v_add_co_u32_e32 v22, vcc, s46, v18
	v_lshlrev_b32_e32 v34, s9, v34
	s_nop 0
	v_addc_co_u32_e32 v23, vcc, 0, v19, vcc
	v_add_u32_e32 v36, s10, v34
	v_mov_b64_e32 v[34:35], s[6:7]
	v_add_co_u32_e32 v30, vcc, s46, v26
	v_mad_u64_u32 v[34:35], s[0:1], v36, s47, v[34:35]
	s_nop 0
	v_addc_co_u32_e32 v31, vcc, 0, v27, vcc
	v_lshl_add_u64 v[34:35], v[34:35], 0, v[86:87]
	v_lshl_add_u64 v[46:47], v[34:35], 0, s[28:29]
	v_add_co_u32_e32 v34, vcc, s60, v34
	global_load_dwordx4 v[2:5], v[6:7], off
	s_nop 0
	global_load_dwordx4 v[6:9], v[6:7], off offset:2048
	v_addc_co_u32_e32 v35, vcc, 0, v35, vcc
	global_load_dwordx4 v[10:13], v[14:15], off
	s_nop 0
	global_load_dwordx4 v[14:17], v[14:15], off offset:2048
	s_nop 0
	global_load_dwordx4 v[18:21], v[22:23], off
	s_nop 0
	global_load_dwordx4 v[22:25], v[22:23], off offset:2048
	s_nop 0
	global_load_dwordx4 v[26:29], v[30:31], off offset:2048
	s_nop 0
	global_load_dwordx4 v[30:33], v[30:31], off
	s_nop 0
	global_load_dwordx4 v[38:41], v[46:47], off offset:64
	global_load_dwordx4 v[42:45], v[46:47], off offset:128
	s_nop 0
	global_load_dwordx4 v[34:37], v[34:35], off offset:2048
	s_nop 0
	global_load_dwordx4 v[46:49], v[46:47], off offset:192
	s_add_i32 s8, s51, 16
	v_or_b32_e32 v93, s8, v1
	s_add_i32 s8, s51, 32
	v_or_b32_e32 v94, s8, v1
	s_add_i32 s8, s51, 48
	v_or_b32_e32 v95, s8, v1
	s_add_i32 s8, s51, 64
	v_or_b32_e32 v96, s8, v1
	s_add_i32 s8, s51, 0x50
	v_or_b32_e32 v97, s8, v1
	s_add_i32 s8, s51, 0x60
	v_or_b32_e32 v98, s8, v1
	s_add_i32 s8, s51, 0x70
	v_cmp_ge_u32_e64 s[10:11], v101, v1
	v_or_b32_e32 v101, 0x81, v132
	v_or_b32_e32 v99, s8, v1
	s_add_i32 s8, s51, 0x80
	v_cmp_gt_u32_e64 s[18:19], v101, v89
	v_or_b32_e32 v101, 0x82, v132
	s_add_i32 s0, 0, 0x11000
	v_or_b32_e32 v136, s51, v1
	v_or3_b32 v90, v90, v132, s51
	s_movk_i32 s1, 0x110
	v_or_b32_e32 v100, s8, v1
	v_cmp_gt_u32_e64 s[20:21], v101, v89
	v_or_b32_e32 v101, 0x83, v132
	v_add_u32_e32 v87, 0, v130
	v_add_u32_e32 v88, s0, v130
	v_add_u32_e32 v86, 0, v86
	v_cmp_eq_u32_e64 s[6:7], 0, v85
	v_mul_u32_u24_e32 v85, 0x110, v83
	v_mul_u32_u24_e32 v83, 0x120, v83
	v_mul_lo_u32 v92, v136, s1
	v_mul_lo_u32 v93, v93, s1
	v_mul_lo_u32 v94, v94, s1
	v_mul_lo_u32 v95, v95, s1
	v_mul_lo_u32 v96, v96, s1
	v_mul_lo_u32 v97, v97, s1
	v_mul_lo_u32 v98, v98, s1
	v_mul_lo_u32 v99, v99, s1
	v_mul_lo_u32 v100, v100, s1
	v_cmp_gt_u32_e64 s[22:23], v101, v89
	v_mul_lo_u32 v89, v90, s26
	v_lshlrev_b32_e32 v130, 1, v82
	v_mbcnt_lo_u32_b32 v82, -1, 0
	v_cmp_ge_u32_e64 s[8:9], v132, v1
	v_add3_u32 v167, s0, v91, v89
	v_add_u32_e32 v168, v87, v85
	v_add_u32_e32 v169, v88, v83
	v_add_u32_e32 v170, v86, v92
	v_add_u32_e32 v171, v86, v93
	v_add_u32_e32 v172, v86, v94
	v_add_u32_e32 v173, v86, v95
	v_add_u32_e32 v174, v86, v96
	v_add_u32_e32 v175, v86, v97
	v_add_u32_e32 v176, v86, v98
	v_add_u32_e32 v177, v86, v99
	v_add_u32_e32 v178, v86, v100
	v_mbcnt_hi_u32_b32 v179, -1, v82
	s_branch .LBB0_477
.LBB0_476:
	s_or_b64 exec, exec, s[34:35]
	v_cmp_gt_i32_e32 vcc, 0, v182
	v_cmp_gt_i32_e64 s[0:1], s49, v182
	s_mov_b32 s48, s61
	s_mov_b32 s100, s101
	s_waitcnt vmcnt(27)
	v_cndmask_b32_e64 v81, v81, 0, vcc
	v_cndmask_b32_e64 v80, v80, 0, vcc
	v_cndmask_b32_e64 v79, v79, 0, vcc
	v_cndmask_b32_e64 v78, v78, 0, vcc
	s_waitcnt vmcnt(26)
	v_cndmask_b32_e64 v73, v73, 0, vcc
	v_cndmask_b32_e64 v72, v72, 0, vcc
	v_cndmask_b32_e64 v71, v71, 0, vcc
	v_cndmask_b32_e64 v70, v70, 0, vcc
	s_waitcnt vmcnt(23)
	v_cndmask_b32_e64 v69, v69, 0, vcc
	v_cndmask_b32_e64 v68, v68, 0, vcc
	v_cndmask_b32_e64 v67, v67, 0, vcc
	v_cndmask_b32_e64 v66, v66, 0, vcc
	s_waitcnt vmcnt(22)
	v_cndmask_b32_e64 v57, v57, 0, vcc
	v_cndmask_b32_e64 v56, v56, 0, vcc
	v_cndmask_b32_e64 v55, v55, 0, vcc
	v_cndmask_b32_e64 v54, v54, 0, vcc
	v_cmp_gt_i32_e32 vcc, s50, v182
	v_cndmask_b32_e64 v77, v77, 0, s[0:1]
	v_cndmask_b32_e64 v76, v76, 0, s[0:1]
	v_cndmask_b32_e64 v75, v75, 0, s[0:1]
	v_cndmask_b32_e64 v74, v74, 0, s[0:1]
	v_cndmask_b32_e64 v65, v65, 0, s[0:1]
	v_cndmask_b32_e64 v64, v64, 0, s[0:1]
	v_cndmask_b32_e64 v63, v63, 0, s[0:1]
	v_cndmask_b32_e64 v62, v62, 0, s[0:1]
	s_waitcnt vmcnt(21)
	v_cndmask_b32_e64 v61, v61, 0, vcc
	v_cndmask_b32_e64 v60, v60, 0, vcc
	v_cndmask_b32_e64 v59, v59, 0, vcc
	v_cndmask_b32_e64 v58, v58, 0, vcc
	s_waitcnt vmcnt(20)
	v_cndmask_b32_e64 v53, v53, 0, vcc
	v_cndmask_b32_e64 v52, v52, 0, vcc
	v_cndmask_b32_e64 v51, v51, 0, vcc
	v_cndmask_b32_e64 v50, v50, 0, vcc
	s_andn2_b64 vcc, exec, s[30:31]
	s_cbranch_vccz .LBB0_479
.LBB0_477:
	s_ashr_i32 s0, s48, 10
	s_lshl_b32 s1, s0, 1
	s_lshr_b32 s31, 64, s1
	s_and_b32 s26, s48, 63
	s_sub_i32 s30, 6, s1
	s_add_i32 s31, s31, -1
	s_and_b32 s34, s31, s26
	s_lshr_b32 s26, s26, s30
	s_add_i32 s101, s100, s33
	s_lshr_b32 s62, s101, 6
	s_mul_i32 s62, s62, 43
	s_lshr_b32 s62, s62, 7
	s_mul_i32 s63, s62, 0xc0
	s_sub_i32 s63, s101, s63
	s_lshr_b32 s66, s63, 4
	s_mul_i32 s66, s66, 43
	s_lshr_b32 s66, s66, 7
	s_mul_i32 s67, s66, 48
	s_sub_i32 s63, s63, s67
	s_lshr_b32 s67, s63, 4
	s_and_b32 s63, s63, 15
	s_lshl_b32 s67, s67, 1
	s_sub_i32 s61, 4, s67
	s_lshr_b32 s98, s63, s61
	s_lshl_b32 s66, s66, s61
	s_lshl_b32 s61, s98, s61
	s_sub_i32 s63, s63, s61
	s_or_b32 s63, s63, s66
	s_lshl_b32 s61, s61, 2
	s_or_b32 s61, s61, s63
	s_lshl_b32 s62, s62, 6
	s_or_b32 s61, s61, s62
	s_lshl_b32 s67, s67, 9
	s_or_b32 s61, s61, s67
	s_cmp_ge_i32 s101, s3
	s_cselect_b64 s[30:31], -1, 0
	s_cmp_lt_i32 s101, s3
	s_cselect_b32 s35, s61, s48
	s_ashr_i32 s63, s35, 9
	s_and_b32 s66, s63, -2
	s_and_b32 s62, s35, 63
	s_sub_i32 s63, 6, s66
	s_lshr_b32 s67, s62, s63
	s_lshr_b32 s63, 64, s66
	s_add_i32 s63, s63, -1
	s_and_b32 s62, s63, s62
	s_lshl_b32 s68, s62, 7
	s_lshl_b32 s62, s35, 4
	s_and_b32 s62, s62, 0x2000
	s_mulk_i32 s62, 0x3000
	s_add_u32 s62, s36, s62
	s_addc_u32 s63, s37, 0
	s_lshl_b32 s35, s35, 2
	s_and_b32 s35, s35, 0x700
	v_add_u32_e32 v182, s68, v133
	s_waitcnt lgkmcnt(0)
	s_barrier
	ds_write_b128 v168, v[78:81]
	ds_write_b128 v169, v[70:73]
	ds_write_b128 v168, v[74:77] offset:8704
	ds_write_b128 v169, v[62:65] offset:9216
	ds_write_b128 v168, v[66:69] offset:17408
	ds_write_b128 v169, v[54:57] offset:18432
	ds_write_b128 v168, v[58:61] offset:26112
	ds_write_b128 v169, v[50:53] offset:27648
	s_waitcnt vmcnt(11)
	ds_write_b128 v168, v[2:5] offset:34816
	s_waitcnt vmcnt(10)
	ds_write_b128 v169, v[6:9] offset:36864
	s_waitcnt vmcnt(9)
	ds_write_b128 v168, v[10:13] offset:43520
	s_waitcnt vmcnt(8)
	ds_write_b128 v169, v[14:17] offset:46080
	s_waitcnt vmcnt(7)
	ds_write_b128 v168, v[18:21] offset:52224
	s_waitcnt vmcnt(6)
	ds_write_b128 v169, v[22:25] offset:55296
	s_waitcnt vmcnt(4)
	ds_write_b128 v168, v[30:33] offset:60928
	ds_write_b128 v169, v[26:29] offset:64512
	s_add_u32 s62, s62, s35
	v_max_i32_e32 v2, 0, v182
	s_addc_u32 s63, s63, 0
	v_lshlrev_b32_e32 v2, s66, v2
	v_lshl_add_u64 v[26:27], s[62:63], 0, v[130:131]
	v_add_u32_e32 v2, s67, v2
	v_mad_i64_i32 v[2:3], s[64:65], v2, s47, v[26:27]
	v_add_co_u32_e32 v2, vcc, s46, v2
	v_max_i32_e32 v10, 0xffffff60, v182
	s_nop 0
	v_addc_co_u32_e32 v3, vcc, 0, v3, vcc
	global_load_dwordx4 v[78:81], v[2:3], off
	global_load_dwordx4 v[70:73], v[2:3], off offset:2048
	v_max_i32_e32 v2, 0xffffffe0, v182
	v_add_lshl_u32 v2, v2, 32, s66
	v_add_u32_e32 v2, s67, v2
	v_mad_i64_i32 v[2:3], s[64:65], v2, s47, v[26:27]
	v_add_co_u32_e32 v2, vcc, s46, v2
	v_add_u32_e32 v10, 0xa0, v10
	s_nop 0
	v_addc_co_u32_e32 v3, vcc, 0, v3, vcc
	global_load_dwordx4 v[74:77], v[2:3], off
	global_load_dwordx4 v[62:65], v[2:3], off offset:2048
	v_or_b32_e32 v2, 64, v182
	v_max_i32_e32 v2, 0, v2
	v_lshlrev_b32_e32 v2, s66, v2
	v_add_u32_e32 v2, s67, v2
	v_mad_i64_i32 v[2:3], s[64:65], v2, s47, v[26:27]
	v_add_co_u32_e32 v2, vcc, s46, v2
	v_lshlrev_b32_e32 v10, s66, v10
	s_nop 0
	v_addc_co_u32_e32 v3, vcc, 0, v3, vcc
	global_load_dwordx4 v[66:69], v[2:3], off
	global_load_dwordx4 v[54:57], v[2:3], off offset:2048
	v_max_i32_e32 v2, 0xffffffa0, v182
	v_add_u32_e32 v2, 0x60, v2
	v_lshlrev_b32_e32 v2, s66, v2
	v_add_u32_e32 v2, s67, v2
	v_mad_i64_i32 v[2:3], s[64:65], v2, s47, v[26:27]
	v_add_co_u32_e32 v2, vcc, s46, v2
	v_max_i32_e32 v18, 0xffffff40, v182
	s_nop 0
	v_addc_co_u32_e32 v3, vcc, 0, v3, vcc
	global_load_dwordx4 v[58:61], v[2:3], off
	global_load_dwordx4 v[50:53], v[2:3], off offset:2048
	v_max_i32_e32 v2, 0xffffff80, v182
	v_add_u32_e32 v2, 0x80, v2
	v_lshlrev_b32_e32 v2, s66, v2
	v_add_u32_e32 v2, s67, v2
	v_mad_i64_i32 v[2:3], s[64:65], v2, s47, v[26:27]
	v_add_co_u32_e32 v6, vcc, s46, v2
	v_add_u32_e32 v10, s67, v10
	v_add_u32_e32 v18, 0xc0, v18
	v_addc_co_u32_e32 v7, vcc, 0, v3, vcc
	v_mad_i64_i32 v[10:11], s[64:65], v10, s47, v[26:27]
	v_lshlrev_b32_e32 v18, s66, v18
	v_max_i32_e32 v28, 0xffffff20, v182
	s_waitcnt vmcnt(9)
	v_mov_b64_e32 v[96:97], v[36:37]
	v_add_co_u32_e32 v14, vcc, s46, v10
	v_add_u32_e32 v18, s67, v18
	v_add_u32_e32 v28, 0xe0, v28
	v_mov_b64_e32 v[94:95], v[34:35]
	v_addc_co_u32_e32 v15, vcc, 0, v11, vcc
	v_mad_i64_i32 v[18:19], s[64:65], v18, s47, v[26:27]
	v_lshlrev_b32_e32 v28, s66, v28
	v_add_u32_e32 v34, s68, v136
	v_add_co_u32_e32 v22, vcc, s46, v18
	v_add_u32_e32 v28, s67, v28
	v_lshlrev_b32_e32 v34, s66, v34
	v_addc_co_u32_e32 v23, vcc, 0, v19, vcc
	v_mad_i64_i32 v[26:27], s[64:65], v28, s47, v[26:27]
	v_add_u32_e32 v36, s67, v34
	v_mov_b64_e32 v[34:35], s[62:63]
	v_add_co_u32_e32 v26, vcc, s46, v26
	v_mad_i64_i32 v[34:35], s[62:63], v36, s47, v[34:35]
	v_mov_b32_e32 v135, v131
	s_waitcnt vmcnt(8)
	v_mov_b64_e32 v[84:85], v[48:49]
	v_addc_co_u32_e32 v27, vcc, 0, v27, vcc
	v_lshl_add_u64 v[34:35], v[34:35], 0, v[134:135]
	v_mov_b64_e32 v[82:83], v[46:47]
	v_lshl_add_u64 v[46:47], v[34:35], 0, s[28:29]
	v_add_co_u32_e32 v34, vcc, s60, v34
	v_mov_b64_e32 v[92:93], v[40:41]
	v_mov_b64_e32 v[88:89], v[44:45]
	v_addc_co_u32_e32 v35, vcc, 0, v35, vcc
	v_mov_b64_e32 v[90:91], v[38:39]
	v_mov_b64_e32 v[86:87], v[42:43]
	global_load_dwordx4 v[2:5], v[6:7], off
	s_nop 0
	global_load_dwordx4 v[6:9], v[6:7], off offset:2048
	s_nop 0
	global_load_dwordx4 v[10:13], v[14:15], off
	s_nop 0
	global_load_dwordx4 v[14:17], v[14:15], off offset:2048
	s_nop 0
	global_load_dwordx4 v[18:21], v[22:23], off
	s_nop 0
	global_load_dwordx4 v[22:25], v[22:23], off offset:2048
	s_nop 0
	global_load_dwordx4 v[30:33], v[26:27], off
	s_nop 0
	global_load_dwordx4 v[26:29], v[26:27], off offset:2048
	s_nop 0
	global_load_dwordx4 v[34:37], v[34:35], off offset:2048
	s_nop 0
	global_load_dwordx4 v[38:41], v[46:47], off offset:64
	global_load_dwordx4 v[42:45], v[46:47], off offset:128
	s_nop 0
	global_load_dwordx4 v[46:49], v[46:47], off offset:192
	s_waitcnt lgkmcnt(0)
	s_barrier
	ds_read_b128 v[98:101], v170
	ds_read_b128 v[102:105], v170 offset:64
	s_waitcnt lgkmcnt(1)
	v_mfma_f32_16x16x32_f16 v[98:101], v[98:101], v[94:97], 0
	ds_read_b128 v[188:191], v177 offset:64
	s_lshl_b32 s34, s34, 7
	s_add_i32 s34, s34, s51
	s_waitcnt lgkmcnt(1)
	v_mfma_f32_16x16x32_f16 v[98:101], v[102:105], v[90:93], v[98:101]
	ds_read_b128 v[102:105], v170 offset:128
	s_sub_i32 s35, 0x7f, s34
	v_cmp_lt_i32_e32 vcc, s35, v132
	s_waitcnt lgkmcnt(0)
	v_mfma_f32_16x16x32_f16 v[98:101], v[102:105], v[86:89], v[98:101]
	ds_read_b128 v[102:105], v170 offset:192
	s_and_b64 vcc, s[8:9], vcc
	s_mov_b32 s62, 0xf149f2ca
	s_waitcnt lgkmcnt(0)
	v_mfma_f32_16x16x32_f16 v[126:129], v[102:105], v[82:85], v[98:101]
	s_nop 2
	ds_read_b128 v[98:101], v171
	ds_read_b128 v[102:105], v171 offset:64
	s_waitcnt lgkmcnt(1)
	v_mfma_f32_16x16x32_f16 v[98:101], v[98:101], v[94:97], 0
	s_waitcnt lgkmcnt(0)
	v_mfma_f32_16x16x32_f16 v[98:101], v[102:105], v[90:93], v[98:101]
	ds_read_b128 v[102:105], v171 offset:128
	s_waitcnt lgkmcnt(0)
	v_mfma_f32_16x16x32_f16 v[98:101], v[102:105], v[86:89], v[98:101]
	ds_read_b128 v[102:105], v171 offset:192
	s_waitcnt lgkmcnt(0)
	v_mfma_f32_16x16x32_f16 v[122:125], v[102:105], v[82:85], v[98:101]
	s_nop 4
	ds_read_b128 v[98:101], v172
	ds_read_b128 v[102:105], v172 offset:64
	s_waitcnt lgkmcnt(1)
	v_mfma_f32_16x16x32_f16 v[98:101], v[98:101], v[94:97], 0
	s_waitcnt lgkmcnt(0)
	v_mfma_f32_16x16x32_f16 v[98:101], v[102:105], v[90:93], v[98:101]
	ds_read_b128 v[102:105], v172 offset:128
	s_waitcnt lgkmcnt(0)
	v_mfma_f32_16x16x32_f16 v[98:101], v[102:105], v[86:89], v[98:101]
	ds_read_b128 v[102:105], v172 offset:192
	s_waitcnt lgkmcnt(0)
	v_mfma_f32_16x16x32_f16 v[118:121], v[102:105], v[82:85], v[98:101]
	s_nop 4
	ds_read_b128 v[98:101], v173
	ds_read_b128 v[102:105], v173 offset:64
	s_waitcnt lgkmcnt(1)
	v_mfma_f32_16x16x32_f16 v[98:101], v[98:101], v[94:97], 0
	s_waitcnt lgkmcnt(0)
	v_mfma_f32_16x16x32_f16 v[98:101], v[102:105], v[90:93], v[98:101]
	ds_read_b128 v[102:105], v173 offset:128
	s_waitcnt lgkmcnt(0)
	v_mfma_f32_16x16x32_f16 v[98:101], v[102:105], v[86:89], v[98:101]
	ds_read_b128 v[102:105], v173 offset:192
	s_waitcnt lgkmcnt(0)
	v_mfma_f32_16x16x32_f16 v[114:117], v[102:105], v[82:85], v[98:101]
	s_nop 4
	ds_read_b128 v[98:101], v174
	ds_read_b128 v[102:105], v174 offset:64
	s_nop 0
	v_mul_f32_e32 v114, 0x3db504f3, v114
	s_waitcnt lgkmcnt(1)
	v_mfma_f32_16x16x32_f16 v[98:101], v[98:101], v[94:97], 0
	s_waitcnt lgkmcnt(0)
	v_mfma_f32_16x16x32_f16 v[98:101], v[102:105], v[90:93], v[98:101]
	ds_read_b128 v[102:105], v174 offset:128
	s_waitcnt lgkmcnt(0)
	v_mfma_f32_16x16x32_f16 v[98:101], v[102:105], v[86:89], v[98:101]
	ds_read_b128 v[102:105], v174 offset:192
	s_waitcnt lgkmcnt(0)
	v_mfma_f32_16x16x32_f16 v[110:113], v[102:105], v[82:85], v[98:101]
	s_nop 4
	ds_read_b128 v[98:101], v175
	ds_read_b128 v[102:105], v175 offset:64
	s_nop 0
	v_mul_f32_e32 v110, 0x3db504f3, v110
	s_waitcnt lgkmcnt(1)
	v_mfma_f32_16x16x32_f16 v[98:101], v[98:101], v[94:97], 0
	v_mul_f32_e32 v111, 0x3db504f3, v111
	v_mul_f32_e32 v112, 0x3db504f3, v112
	s_waitcnt lgkmcnt(0)
	v_mfma_f32_16x16x32_f16 v[98:101], v[102:105], v[90:93], v[98:101]
	ds_read_b128 v[102:105], v175 offset:128
	s_waitcnt lgkmcnt(0)
	v_mfma_f32_16x16x32_f16 v[98:101], v[102:105], v[86:89], v[98:101]
	ds_read_b128 v[102:105], v175 offset:192
	s_waitcnt lgkmcnt(0)
	v_mfma_f32_16x16x32_f16 v[106:109], v[102:105], v[82:85], v[98:101]
	s_nop 4
	ds_read_b128 v[98:101], v176
	ds_read_b128 v[102:105], v176 offset:64
	s_nop 0
	v_mul_f32_e32 v106, 0x3db504f3, v106
	s_waitcnt lgkmcnt(1)
	v_mfma_f32_16x16x32_f16 v[98:101], v[98:101], v[94:97], 0
	v_mul_f32_e32 v107, 0x3db504f3, v107
	v_mul_f32_e32 v108, 0x3db504f3, v108
	v_mul_f32_e32 v109, 0x3db504f3, v109
	s_waitcnt lgkmcnt(0)
	v_mfma_f32_16x16x32_f16 v[98:101], v[102:105], v[90:93], v[98:101]
	ds_read_b128 v[102:105], v176 offset:128
	s_waitcnt lgkmcnt(0)
	v_mfma_f32_16x16x32_f16 v[98:101], v[102:105], v[86:89], v[98:101]
	ds_read_b128 v[102:105], v176 offset:192
	s_waitcnt lgkmcnt(0)
	v_mfma_f32_16x16x32_f16 v[102:105], v[102:105], v[82:85], v[98:101]
	s_nop 4
	ds_read_b128 v[98:101], v177
	s_nop 1
	v_mul_f32_e32 v102, 0x3db504f3, v102
	s_waitcnt lgkmcnt(0)
	v_mfma_f32_16x16x32_f16 v[98:101], v[98:101], v[94:97], 0
	v_mfma_f32_16x16x32_f16 v[98:101], v[188:191], v[90:93], v[98:101]
	ds_read_b128 v[188:191], v177 offset:128
	s_waitcnt lgkmcnt(0)
	v_mfma_f32_16x16x32_f16 v[98:101], v[188:191], v[86:89], v[98:101]
	ds_read_b128 v[188:191], v177 offset:192
	s_waitcnt lgkmcnt(0)
	v_mfma_f32_16x16x32_f16 v[98:101], v[188:191], v[82:85], v[98:101]
	ds_read_b128 v[188:191], v178
	s_nop 6
	v_mul_f32_e32 v98, 0x3db504f3, v98
	s_waitcnt lgkmcnt(0)
	v_mfma_f32_16x16x32_f16 v[94:97], v[188:191], v[94:97], 0
	ds_read_b128 v[188:191], v178 offset:64
	s_waitcnt lgkmcnt(0)
	v_mfma_f32_16x16x32_f16 v[90:93], v[188:191], v[90:93], v[94:97]
	s_nop 4
	ds_read_b128 v[94:97], v178 offset:128
	s_waitcnt lgkmcnt(0)
	v_mfma_f32_16x16x32_f16 v[86:89], v[94:97], v[86:89], v[90:93]
	s_nop 2
	ds_read_b128 v[90:93], v178 offset:192
	v_mul_f32_e32 v94, 0x3db504f3, v125
	v_mul_f32_e32 v95, 0x3db504f3, v118
	s_waitcnt lgkmcnt(0)
	v_mfma_f32_16x16x32_f16 v[82:85], v[90:93], v[82:85], v[86:89]
	s_nop 2
	v_mul_f32_e32 v86, 0x3db504f3, v126
	v_cndmask_b32_e32 v86, v180, v86, vcc
	v_cmp_le_i32_e32 vcc, s35, v132
	s_and_b64 vcc, s[10:11], vcc
	v_mul_f32_e32 v87, 0x3db504f3, v127
	v_cndmask_b32_e32 v87, v180, v87, vcc
	v_cmp_lt_i32_e32 vcc, s35, v137
	s_and_b64 vcc, s[12:13], vcc
	v_mul_f32_e32 v89, 0x3db504f3, v128
	v_cndmask_b32_e32 v89, v180, v89, vcc
	v_cmp_lt_i32_e32 vcc, s35, v138
	s_and_b64 vcc, s[14:15], vcc
	v_mul_f32_e32 v90, 0x3db504f3, v129
	v_cndmask_b32_e32 v90, v180, v90, vcc
	v_cmp_lt_i32_e32 vcc, s35, v139
	v_mul_f32_e32 v91, 0x3db504f3, v122
	v_mul_f32_e32 v92, 0x3db504f3, v123
	v_cndmask_b32_e32 v91, v180, v91, vcc
	v_cmp_lt_i32_e32 vcc, s35, v140
	v_mul_f32_e32 v93, 0x3db504f3, v124
	v_mul_f32_e32 v96, 0x3db504f3, v119
	v_cndmask_b32_e32 v92, v180, v92, vcc
	v_cmp_lt_i32_e32 vcc, s35, v141
	v_mul_f32_e32 v97, 0x3db504f3, v120
	v_mul_f32_e32 v118, 0x3db504f3, v121
	v_cndmask_b32_e32 v93, v180, v93, vcc
	v_cmp_lt_i32_e32 vcc, s35, v142
	v_max3_f32 v88, v86, s62, v87
	v_max3_f32 v88, v88, v89, v90
	v_cndmask_b32_e32 v94, v180, v94, vcc
	v_cmp_lt_i32_e32 vcc, s35, v143
	v_max3_f32 v88, v88, v91, v92
	v_max3_f32 v88, v88, v93, v94
	v_cndmask_b32_e32 v95, v180, v95, vcc
	v_cmp_lt_i32_e32 vcc, s35, v144
	v_mul_f32_e32 v82, 0x3db504f3, v82
	v_mul_f32_e32 v83, 0x3db504f3, v83
	v_cndmask_b32_e32 v96, v180, v96, vcc
	v_cmp_lt_i32_e32 vcc, s35, v145
	v_max3_f32 v88, v88, v95, v96
	v_cndmask_b32_e64 v82, v82, v180, s[16:17]
	v_cndmask_b32_e32 v97, v180, v97, vcc
	v_cmp_lt_i32_e32 vcc, s35, v146
	v_cndmask_b32_e64 v83, v83, v180, s[18:19]
	v_mul_f32_e32 v84, 0x3db504f3, v84
	v_cndmask_b32_e32 v118, v180, v118, vcc
	v_cmp_lt_i32_e32 vcc, s35, v147
	v_max3_f32 v88, v88, v97, v118
	v_mul_f32_e32 v85, 0x3db504f3, v85
	v_cndmask_b32_e32 v119, v180, v114, vcc
	v_cmp_lt_i32_e32 vcc, s35, v148
	v_mul_f32_e32 v114, 0x3db504f3, v115
	v_cndmask_b32_e64 v84, v84, v180, s[20:21]
	v_cndmask_b32_e32 v120, v180, v114, vcc
	v_cmp_lt_i32_e32 vcc, s35, v149
	v_mul_f32_e32 v114, 0x3db504f3, v116
	v_max3_f32 v88, v88, v119, v120
	v_cndmask_b32_e32 v116, v180, v114, vcc
	v_cmp_lt_i32_e32 vcc, s35, v150
	v_mul_f32_e32 v114, 0x3db504f3, v117
	v_cndmask_b32_e64 v183, v85, v180, s[22:23]
	v_cndmask_b32_e32 v117, v180, v114, vcc
	v_cmp_lt_i32_e32 vcc, s35, v151
	v_max3_f32 v88, v88, v116, v117
	s_nop 0
	v_cndmask_b32_e32 v110, v180, v110, vcc
	v_cmp_lt_i32_e32 vcc, s35, v152
	s_nop 1
	v_cndmask_b32_e32 v111, v180, v111, vcc
	v_cmp_lt_i32_e32 vcc, s35, v153
	v_max3_f32 v88, v88, v110, v111
	s_nop 0
	v_cndmask_b32_e32 v121, v180, v112, vcc
	v_cmp_lt_i32_e32 vcc, s35, v154
	v_mul_f32_e32 v112, 0x3db504f3, v113
	s_nop 0
	v_cndmask_b32_e32 v122, v180, v112, vcc
	v_cmp_lt_i32_e32 vcc, s35, v155
	v_max3_f32 v88, v88, v121, v122
	s_nop 0
	v_cndmask_b32_e32 v106, v180, v106, vcc
	v_cmp_lt_i32_e32 vcc, s35, v156
	s_nop 1
	v_cndmask_b32_e32 v107, v180, v107, vcc
	v_cmp_lt_i32_e32 vcc, s35, v157
	v_max3_f32 v88, v88, v106, v107
	s_nop 0
	v_cndmask_b32_e32 v108, v180, v108, vcc
	v_cmp_lt_i32_e32 vcc, s35, v158
	s_nop 1
	v_cndmask_b32_e32 v109, v180, v109, vcc
	v_cmp_lt_i32_e32 vcc, s35, v159
	v_max3_f32 v88, v88, v108, v109
	s_nop 0
	v_cndmask_b32_e32 v123, v180, v102, vcc
	v_cmp_lt_i32_e32 vcc, s35, v160
	v_mul_f32_e32 v102, 0x3db504f3, v103
	s_nop 0
	v_cndmask_b32_e32 v124, v180, v102, vcc
	v_cmp_lt_i32_e32 vcc, s35, v161
	v_mul_f32_e32 v102, 0x3db504f3, v104
	v_max3_f32 v88, v88, v123, v124
	v_cndmask_b32_e32 v125, v180, v102, vcc
	v_cmp_lt_i32_e32 vcc, s35, v162
	v_mul_f32_e32 v102, 0x3db504f3, v105
	s_nop 0
	v_cndmask_b32_e32 v126, v180, v102, vcc
	v_cmp_lt_i32_e32 vcc, s35, v163
	v_max3_f32 v88, v88, v125, v126
	s_nop 0
	v_cndmask_b32_e32 v127, v180, v98, vcc
	v_cmp_lt_i32_e32 vcc, s35, v164
	v_mul_f32_e32 v98, 0x3db504f3, v99
	s_nop 0
	v_cndmask_b32_e32 v128, v180, v98, vcc
	v_cmp_lt_i32_e32 vcc, s35, v165
	v_mul_f32_e32 v98, 0x3db504f3, v100
	v_max3_f32 v88, v88, v127, v128
	v_cndmask_b32_e32 v129, v180, v98, vcc
	v_cmp_lt_i32_e32 vcc, s35, v166
	v_mul_f32_e32 v98, 0x3db504f3, v101
	s_nop 0
	v_cndmask_b32_e32 v135, v180, v98, vcc
	v_max3_f32 v88, v88, v129, v135
	v_max3_f32 v88, v88, v82, v83
	v_and_b32_e32 v98, 64, v179
	v_max3_f32 v85, v88, v84, v183
	v_xor_b32_e32 v88, 16, v179
	v_add_u32_e32 v98, 64, v98
	v_cmp_lt_i32_e32 vcc, v88, v98
	s_nop 1
	v_cndmask_b32_e32 v88, v179, v88, vcc
	v_lshlrev_b32_e32 v184, 2, v88
	ds_bpermute_b32 v88, v184, v85
	s_waitcnt lgkmcnt(0)
	v_max_f32_e32 v88, v88, v88
	v_max_f32_e32 v85, v85, v88
	v_xor_b32_e32 v88, 32, v179
	v_cmp_lt_i32_e32 vcc, v88, v98
	s_nop 1
	v_cndmask_b32_e32 v88, v179, v88, vcc
	v_lshlrev_b32_e32 v185, 2, v88
	ds_bpermute_b32 v88, v185, v85
	s_waitcnt lgkmcnt(0)
	v_max_f32_e32 v88, v88, v88
	v_max_f32_e32 v85, v85, v88
	v_sub_f32_e32 v86, v86, v85
	v_mul_f32_e32 v86, 0x3fb8aa3b, v86
	v_exp_f32_e32 v187, v86
	v_sub_f32_e32 v86, v87, v85
	v_sub_f32_e32 v87, v91, v85
	v_mul_f32_e32 v87, 0x3fb8aa3b, v87
	v_exp_f32_e32 v105, v87
	v_sub_f32_e32 v87, v92, v85
	v_mul_f32_e32 v87, 0x3fb8aa3b, v87
	v_exp_f32_e32 v114, v87
	v_sub_f32_e32 v87, v93, v85
	v_mul_f32_e32 v87, 0x3fb8aa3b, v87
	v_exp_f32_e32 v115, v87
	v_sub_f32_e32 v87, v94, v85
	v_mul_f32_e32 v87, 0x3fb8aa3b, v87
	v_exp_f32_e32 v188, v87
	v_sub_f32_e32 v87, v95, v85
	v_mul_f32_e32 v87, 0x3fb8aa3b, v87
	v_exp_f32_e32 v208, v87
	v_sub_f32_e32 v87, v96, v85
	v_mul_f32_e32 v87, 0x3fb8aa3b, v87
	v_exp_f32_e32 v100, v87
	v_sub_f32_e32 v87, v97, v85
	v_mul_f32_e32 v87, 0x3fb8aa3b, v87
	v_exp_f32_e32 v101, v87
	v_sub_f32_e32 v87, v118, v85
	v_mul_f32_e32 v86, 0x3fb8aa3b, v86
	v_mul_f32_e32 v87, 0x3fb8aa3b, v87
	v_exp_f32_e32 v112, v86
	v_sub_f32_e32 v86, v89, v85
	v_exp_f32_e32 v98, v87
	v_sub_f32_e32 v87, v119, v85
	v_mul_f32_e32 v86, 0x3fb8aa3b, v86
	v_mul_f32_e32 v87, 0x3fb8aa3b, v87
	v_exp_f32_e32 v113, v86
	v_sub_f32_e32 v86, v90, v85
	v_exp_f32_e32 v99, v87
	v_sub_f32_e32 v87, v120, v85
	v_mul_f32_e32 v86, 0x3fb8aa3b, v86
	v_mul_f32_e32 v87, 0x3fb8aa3b, v87
	v_exp_f32_e32 v104, v86
	v_exp_f32_e32 v102, v87
	v_sub_f32_e32 v87, v116, v85
	v_add_f32_e32 v86, 0, v187
	v_mul_f32_e32 v87, 0x3fb8aa3b, v87
	v_add_f32_e32 v86, v112, v86
	v_exp_f32_e32 v103, v87
	v_sub_f32_e32 v87, v117, v85
	v_add_f32_e32 v86, v113, v86
	v_mul_f32_e32 v87, 0x3fb8aa3b, v87
	v_add_f32_e32 v86, v104, v86
	v_exp_f32_e32 v209, v87
	v_sub_f32_e32 v87, v110, v85
	v_add_f32_e32 v86, v105, v86
	v_mul_f32_e32 v87, 0x3fb8aa3b, v87
	v_add_f32_e32 v86, v114, v86
	v_exp_f32_e32 v210, v87
	v_sub_f32_e32 v87, v111, v85
	v_add_f32_e32 v86, v115, v86
	v_mul_f32_e32 v87, 0x3fb8aa3b, v87
	v_add_f32_e32 v86, v188, v86
	v_exp_f32_e32 v94, v87
	v_sub_f32_e32 v87, v121, v85
	v_add_f32_e32 v86, v208, v86
	v_mul_f32_e32 v87, 0x3fb8aa3b, v87
	v_add_f32_e32 v86, v100, v86
	v_exp_f32_e32 v95, v87
	v_sub_f32_e32 v87, v122, v85
	v_add_f32_e32 v86, v101, v86
	v_mul_f32_e32 v87, 0x3fb8aa3b, v87
	v_add_f32_e32 v86, v98, v86
	v_exp_f32_e32 v92, v87
	v_sub_f32_e32 v87, v106, v85
	v_add_f32_e32 v86, v99, v86
	v_mul_f32_e32 v87, 0x3fb8aa3b, v87
	v_add_f32_e32 v86, v102, v86
	v_exp_f32_e32 v93, v87
	v_sub_f32_e32 v87, v107, v85
	v_add_f32_e32 v86, v103, v86
	v_mul_f32_e32 v87, 0x3fb8aa3b, v87
	v_add_f32_e32 v86, v209, v86
	v_exp_f32_e32 v96, v87
	v_sub_f32_e32 v87, v108, v85
	v_add_f32_e32 v86, v210, v86
	v_mul_f32_e32 v87, 0x3fb8aa3b, v87
	v_add_f32_e32 v86, v94, v86
	v_exp_f32_e32 v97, v87
	v_sub_f32_e32 v87, v109, v85
	v_add_f32_e32 v86, v95, v86
	v_mul_f32_e32 v87, 0x3fb8aa3b, v87
	v_add_f32_e32 v86, v92, v86
	v_exp_f32_e32 v111, v87
	v_add_f32_e32 v86, v93, v86
	v_add_f32_e32 v86, v96, v86
	v_add_f32_e32 v86, v97, v86
	v_add_f32_e32 v87, v111, v86
	v_sub_f32_e32 v86, v123, v85
	v_mul_f32_e32 v86, 0x3fb8aa3b, v86
	v_exp_f32_e32 v109, v86
	v_sub_f32_e32 v86, v124, v85
	v_mul_f32_e32 v86, 0x3fb8aa3b, v86
	v_exp_f32_e32 v88, v86
	v_sub_f32_e32 v86, v125, v85
	v_mul_f32_e32 v86, 0x3fb8aa3b, v86
	v_exp_f32_e32 v89, v86
	v_sub_f32_e32 v86, v126, v85
	v_mul_f32_e32 v86, 0x3fb8aa3b, v86
	v_exp_f32_e32 v86, v86
	v_add_f32_e32 v87, v109, v87
	v_add_f32_e32 v87, v88, v87
	v_add_f32_e32 v87, v89, v87
	v_add_f32_e32 v106, v86, v87
	v_sub_f32_e32 v87, v127, v85
	v_mul_f32_e32 v87, 0x3fb8aa3b, v87
	v_sub_f32_e32 v90, v128, v85
	v_exp_f32_e32 v87, v87
	v_mul_f32_e32 v90, 0x3fb8aa3b, v90
	v_sub_f32_e32 v91, v129, v85
	v_exp_f32_e32 v90, v90
	v_mul_f32_e32 v91, 0x3fb8aa3b, v91
	v_sub_f32_e32 v107, v135, v85
	v_sub_f32_e32 v82, v82, v85
	v_exp_f32_e32 v91, v91
	v_mul_f32_e32 v107, 0x3fb8aa3b, v107
	v_mul_f32_e32 v82, 0x3fb8aa3b, v82
	v_exp_f32_e32 v110, v107
	v_exp_f32_e32 v108, v82
	v_sub_f32_e32 v82, v83, v85
	v_add_f32_e32 v106, v87, v106
	v_mul_f32_e32 v82, 0x3fb8aa3b, v82
	v_sub_f32_e32 v83, v84, v85
	v_add_f32_e32 v106, v90, v106
	v_exp_f32_e32 v82, v82
	v_mul_f32_e32 v83, 0x3fb8aa3b, v83
	v_sub_f32_e32 v84, v183, v85
	v_add_f32_e32 v106, v91, v106
	v_exp_f32_e32 v83, v83
	v_mul_f32_e32 v84, 0x3fb8aa3b, v84
	v_add_f32_e32 v106, v110, v106
	v_exp_f32_e32 v107, v84
	v_add_f32_e32 v84, v108, v106
	v_add_f32_e32 v84, v82, v84
	v_add_f32_e32 v84, v83, v84
	v_add_f32_e32 v84, v107, v84
	ds_bpermute_b32 v106, v184, v84
	s_waitcnt lgkmcnt(0)
	v_add_f32_e32 v84, v84, v106
	ds_bpermute_b32 v106, v185, v84
	s_waitcnt lgkmcnt(0)
	v_add_f32_e32 v106, v84, v106
	v_div_scale_f32 v84, s[62:63], v106, v106, 1.0
	v_rcp_f32_e32 v116, v84
	s_nop 0
	v_fma_f32 v117, -v84, v116, 1.0
	v_fmac_f32_e32 v116, v117, v116
	v_div_scale_f32 v117, vcc, 1.0, v106, 1.0
	v_mul_f32_e32 v118, v117, v116
	v_fma_f32 v119, -v84, v118, v117
	v_fmac_f32_e32 v118, v119, v116
	v_fma_f32 v84, -v84, v118, v117
	v_div_fmas_f32 v84, v84, v116, v118
	v_div_fixup_f32 v84, v84, v106, 1.0
	v_pk_mul_f32 v[112:113], v[112:113], v[84:85] op_sel_hi:[1,0]
	v_fma_mixlo_f16 v116, v187, v84, 0
	v_cvt_pk_f16_f32 v113, v112, v113
	v_pack_b32_f16 v112, v116, v113
	ds_read_b64_tr_b16 v[118:119], v167 offset:4608
	ds_read_b64_tr_b16 v[116:117], v167
	ds_read_b64_tr_b16 v[120:121], v167 offset:32
	ds_read_b64_tr_b16 v[122:123], v167 offset:4640
	v_pk_mul_f32 v[114:115], v[114:115], v[84:85] op_sel_hi:[1,0]
	v_pk_mul_f32 v[104:105], v[104:105], v[84:85] op_sel_hi:[1,0]
	v_cvt_pk_f16_f32 v115, v114, v115
	v_cvt_pk_f16_f32 v104, v104, v105
	v_alignbit_b32 v114, v115, v104, 16
	v_lshrrev_b32_e32 v115, 16, v115
	v_fma_mixhi_f16 v115, v188, v84, 0
	ds_read_b64_tr_b16 v[124:125], v167 offset:64
	ds_read_b64_tr_b16 v[126:127], v167 offset:4672
	ds_read_b64_tr_b16 v[188:189], v167 offset:96
	ds_read_b64_tr_b16 v[190:191], v167 offset:4704
	ds_read_b64_tr_b16 v[192:193], v167 offset:128
	ds_read_b64_tr_b16 v[194:195], v167 offset:4736
	ds_read_b64_tr_b16 v[196:197], v167 offset:160
	ds_read_b64_tr_b16 v[198:199], v167 offset:4768
	ds_read_b64_tr_b16 v[200:201], v167 offset:192
	ds_read_b64_tr_b16 v[202:203], v167 offset:4800
	ds_read_b64_tr_b16 v[204:205], v167 offset:224
	ds_read_b64_tr_b16 v[206:207], v167 offset:4832
	v_alignbit_b32 v113, v104, v113, 16
	v_pk_mul_f32 v[102:103], v[102:103], v[84:85] op_sel_hi:[1,0]
	v_pk_mul_f32 v[98:99], v[98:99], v[84:85] op_sel_hi:[1,0]
	s_waitcnt lgkmcnt(14)
	v_mfma_f32_16x16x32_f16 v[116:119], v[116:119], v[112:115], 0
	v_mul_f32_e64 v100, v100, v84
	v_mul_f32_e64 v101, v101, v84
	v_cvt_pk_f16_f32 v103, v102, v103
	v_cvt_pk_f16_f32 v98, v98, v99
	s_waitcnt lgkmcnt(12)
	v_mfma_f32_16x16x32_f16 v[120:123], v[120:123], v[112:115], 0
	v_fma_mixlo_f16 v104, v208, v84, 0
	v_cvt_pk_f16_f32 v101, v100, v101
	v_alignbit_b32 v102, v103, v98, 16
	s_waitcnt lgkmcnt(10)
	v_mfma_f32_16x16x32_f16 v[124:127], v[124:127], v[112:115], 0
	v_lshrrev_b32_e32 v103, 16, v103
	v_pack_b32_f16 v100, v104, v101
	v_alignbit_b32 v101, v98, v101, 16
	s_waitcnt lgkmcnt(8)
	v_mfma_f32_16x16x32_f16 v[188:191], v[188:191], v[112:115], 0
	v_fma_mixhi_f16 v103, v209, v84, 0
	v_pk_mul_f32 v[94:95], v[94:95], v[84:85] op_sel_hi:[1,0]
	v_pk_mul_f32 v[96:97], v[96:97], v[84:85] op_sel_hi:[1,0]
	s_waitcnt lgkmcnt(6)
	v_mfma_f32_16x16x32_f16 v[192:195], v[192:195], v[112:115], 0
	v_cvt_pk_f16_f32 v95, v94, v95
	v_pk_mul_f32 v[92:93], v[92:93], v[84:85] op_sel_hi:[1,0]
	v_cvt_pk_f16_f32 v97, v96, v97
	s_waitcnt lgkmcnt(4)
	v_mfma_f32_16x16x32_f16 v[196:199], v[196:199], v[112:115], 0
	v_cvt_pk_f16_f32 v92, v92, v93
	v_alignbit_b32 v96, v97, v92, 16
	v_lshrrev_b32_e32 v97, 16, v97
	s_waitcnt lgkmcnt(2)
	v_mfma_f32_16x16x32_f16 v[200:203], v[200:203], v[112:115], 0
	v_fma_mixhi_f16 v97, v111, v84, 0
	v_pk_mul_f32 v[88:89], v[88:89], v[84:85] op_sel_hi:[1,0]
	v_pk_mul_f32 v[90:91], v[90:91], v[84:85] op_sel_hi:[1,0]
	s_waitcnt lgkmcnt(0)
	v_mfma_f32_16x16x32_f16 v[112:115], v[204:207], v[112:115], 0
	ds_read_b64_tr_b16 v[204:205], v167 offset:9216
	ds_read_b64_tr_b16 v[206:207], v167 offset:13824
	v_cvt_pk_f16_f32 v89, v88, v89
	v_pk_mul_f32 v[86:87], v[86:87], v[84:85] op_sel_hi:[1,0]
	s_waitcnt lgkmcnt(0)
	v_mfma_f32_16x16x32_f16 v[116:119], v[204:207], v[100:103], v[116:119]
	ds_read_b64_tr_b16 v[204:205], v167 offset:9248
	ds_read_b64_tr_b16 v[206:207], v167 offset:13856
	v_cvt_pk_f16_f32 v91, v90, v91
	v_cvt_pk_f16_f32 v86, v86, v87
	s_waitcnt lgkmcnt(0)
	v_mfma_f32_16x16x32_f16 v[120:123], v[204:207], v[100:103], v[120:123]
	ds_read_b64_tr_b16 v[204:205], v167 offset:9280
	ds_read_b64_tr_b16 v[206:207], v167 offset:13888
	v_alignbit_b32 v90, v91, v86, 16
	v_lshrrev_b32_e32 v91, 16, v91
	s_waitcnt lgkmcnt(0)
	v_mfma_f32_16x16x32_f16 v[124:127], v[204:207], v[100:103], v[124:127]
	ds_read_b64_tr_b16 v[204:205], v167 offset:9312
	ds_read_b64_tr_b16 v[206:207], v167 offset:13920
	v_fma_mixhi_f16 v91, v110, v84, 0
	v_pk_mul_f32 v[82:83], v[82:83], v[84:85] op_sel_hi:[1,0]
	s_waitcnt lgkmcnt(0)
	v_mfma_f32_16x16x32_f16 v[188:191], v[204:207], v[100:103], v[188:191]
	ds_read_b64_tr_b16 v[204:205], v167 offset:9344
	ds_read_b64_tr_b16 v[206:207], v167 offset:13952
	v_cvt_pk_f16_f32 v82, v82, v83
	s_waitcnt lgkmcnt(0)
	v_mfma_f32_16x16x32_f16 v[192:195], v[204:207], v[100:103], v[192:195]
	ds_read_b64_tr_b16 v[204:205], v167 offset:9376
	ds_read_b64_tr_b16 v[206:207], v167 offset:13984
	s_waitcnt lgkmcnt(0)
	v_mfma_f32_16x16x32_f16 v[196:199], v[204:207], v[100:103], v[196:199]
	ds_read_b64_tr_b16 v[204:205], v167 offset:9408
	ds_read_b64_tr_b16 v[206:207], v167 offset:14016
	s_waitcnt lgkmcnt(0)
	v_mfma_f32_16x16x32_f16 v[200:203], v[204:207], v[100:103], v[200:203]
	ds_read_b64_tr_b16 v[204:205], v167 offset:9440
	ds_read_b64_tr_b16 v[206:207], v167 offset:14048
	s_waitcnt lgkmcnt(0)
	v_mfma_f32_16x16x32_f16 v[98:101], v[204:207], v[100:103], v[112:115]
	v_fma_mixlo_f16 v102, v210, v84, 0
	v_pack_b32_f16 v94, v102, v95
	ds_read_b64_tr_b16 v[102:103], v167 offset:18432
	ds_read_b64_tr_b16 v[104:105], v167 offset:23040
	ds_read_b64_tr_b16 v[112:113], v167 offset:18464
	ds_read_b64_tr_b16 v[114:115], v167 offset:23072
	v_alignbit_b32 v95, v92, v95, 16
	s_waitcnt lgkmcnt(2)
	s_nop 0
	v_mfma_f32_16x16x32_f16 v[102:105], v[102:105], v[94:97], v[116:119]
	s_nop 2
	ds_read_b64_tr_b16 v[116:117], v167 offset:18496
	ds_read_b64_tr_b16 v[118:119], v167 offset:23104
	s_waitcnt lgkmcnt(2)
	v_mfma_f32_16x16x32_f16 v[112:115], v[112:115], v[94:97], v[120:123]
	s_nop 2
	ds_read_b64_tr_b16 v[120:121], v167 offset:18528
	ds_read_b64_tr_b16 v[122:123], v167 offset:23136
	s_waitcnt lgkmcnt(2)
	v_mfma_f32_16x16x32_f16 v[116:119], v[116:119], v[94:97], v[124:127]
	s_nop 2
	ds_read_b64_tr_b16 v[124:125], v167 offset:18560
	ds_read_b64_tr_b16 v[126:127], v167 offset:23168
	s_waitcnt lgkmcnt(2)
	v_mfma_f32_16x16x32_f16 v[120:123], v[120:123], v[94:97], v[188:191]
	s_nop 2
	ds_read_b64_tr_b16 v[188:189], v167 offset:18592
	ds_read_b64_tr_b16 v[190:191], v167 offset:23200
	s_waitcnt lgkmcnt(2)
	v_mfma_f32_16x16x32_f16 v[124:127], v[124:127], v[94:97], v[192:195]
	s_nop 2
	ds_read_b64_tr_b16 v[192:193], v167 offset:18624
	ds_read_b64_tr_b16 v[194:195], v167 offset:23232
	s_waitcnt lgkmcnt(2)
	v_mfma_f32_16x16x32_f16 v[188:191], v[188:191], v[94:97], v[196:199]
	s_nop 2
	ds_read_b64_tr_b16 v[196:197], v167 offset:18656
	ds_read_b64_tr_b16 v[198:199], v167 offset:23264
	s_waitcnt lgkmcnt(2)
	v_mfma_f32_16x16x32_f16 v[192:195], v[192:195], v[94:97], v[200:203]
	s_waitcnt lgkmcnt(0)
	v_mfma_f32_16x16x32_f16 v[92:95], v[196:199], v[94:97], v[98:101]
	v_fma_mixlo_f16 v96, v109, v84, 0
	v_pack_b32_f16 v88, v96, v89
	ds_read_b64_tr_b16 v[96:97], v167 offset:27648
	ds_read_b64_tr_b16 v[98:99], v167 offset:32256
	v_alignbit_b32 v89, v86, v89, 16
	s_waitcnt lgkmcnt(0)
	s_nop 0
	v_mfma_f32_16x16x32_f16 v[96:99], v[96:99], v[88:91], v[102:105]
	ds_read_b64_tr_b16 v[100:101], v167 offset:27680
	s_nop 1
	ds_read_b64_tr_b16 v[102:103], v167 offset:32288
	v_mov_b32_e32 v104, v131
	v_mov_b32_e32 v105, v131
	s_waitcnt lgkmcnt(0)
	v_mfma_f32_16x16x32_f16 v[100:103], v[100:103], v[88:91], v[112:115]
	ds_read_b64_tr_b16 v[110:111], v167 offset:27712
	s_nop 1
	ds_read_b64_tr_b16 v[112:113], v167 offset:32320
	s_waitcnt lgkmcnt(0)
	v_mfma_f32_16x16x32_f16 v[110:113], v[110:113], v[88:91], v[116:119]
	ds_read_b64_tr_b16 v[114:115], v167 offset:27744
	s_nop 1
	ds_read_b64_tr_b16 v[116:117], v167 offset:32352
	s_waitcnt lgkmcnt(0)
	v_mfma_f32_16x16x32_f16 v[114:117], v[114:117], v[88:91], v[120:123]
	ds_read_b64_tr_b16 v[118:119], v167 offset:27776
	s_nop 1
	ds_read_b64_tr_b16 v[120:121], v167 offset:32384
	s_waitcnt lgkmcnt(0)
	v_mfma_f32_16x16x32_f16 v[118:121], v[118:121], v[88:91], v[124:127]
	ds_read_b64_tr_b16 v[122:123], v167 offset:27808
	s_nop 1
	ds_read_b64_tr_b16 v[124:125], v167 offset:32416
	ds_read_b64_tr_b16 v[126:127], v167 offset:27840
	ds_read_b64_tr_b16 v[128:129], v167 offset:32448
	s_waitcnt lgkmcnt(2)
	v_mfma_f32_16x16x32_f16 v[122:125], v[122:125], v[88:91], v[188:191]
	s_nop 2
	ds_read_b64_tr_b16 v[188:189], v167 offset:27872
	ds_read_b64_tr_b16 v[190:191], v167 offset:32480
	s_waitcnt lgkmcnt(2)
	v_mfma_f32_16x16x32_f16 v[126:129], v[126:129], v[88:91], v[192:195]
	s_waitcnt lgkmcnt(0)
	v_mfma_f32_16x16x32_f16 v[86:89], v[188:191], v[88:91], v[92:95]
	ds_read_b64_tr_b16 v[90:91], v167 offset:36864
	v_lshrrev_b32_e32 v189, 16, v82
	v_fma_mixhi_f16 v189, v107, v84, 0
	v_fma_mixlo_f16 v92, v108, v84, 0
	v_pack_b32_f16 v188, v92, v82
	v_mov_b32_e32 v92, v131
	v_mov_b32_e32 v93, v131
	ds_read_b64_tr_b16 v[94:95], v167 offset:36896
	ds_read_b64_tr_b16 v[108:109], v167 offset:36992
	v_mov_b32_e32 v190, v131
	v_mov_b32_e32 v191, v131
	v_or_b32_e32 v82, s34, v1
	v_lshlrev_b32_e32 v82, s1, v82
	s_waitcnt lgkmcnt(2)
	v_mfma_f32_16x16x32_f16 v[90:93], v[90:93], v[188:191], v[96:99]
	v_add_u32_e32 v82, s26, v82
	s_ashr_i32 s1, s0, 31
	s_lshl_b32 s26, s48, 4
	v_mov_b32_e32 v96, v131
	v_mov_b32_e32 v97, v131
	ds_read_b64_tr_b16 v[98:99], v167 offset:36928
	s_and_b32 s26, s26, 0x2000
	s_waitcnt lgkmcnt(2)
	v_mfma_f32_16x16x32_f16 v[94:97], v[94:97], v[188:191], v[100:103]
	s_lshl_b64 s[34:35], s[0:1], 25
	s_nop 1
	v_mov_b32_e32 v100, v131
	v_mov_b32_e32 v101, v131
	ds_read_b64_tr_b16 v[102:103], v167 offset:36960
	s_waitcnt lgkmcnt(0)
	v_mfma_f32_16x16x32_f16 v[102:105], v[102:105], v[188:191], v[114:117]
	s_nop 2
	v_mov_b32_e32 v114, v131
	v_mov_b32_e32 v115, v131
	ds_read_b64_tr_b16 v[116:117], v167 offset:37056
	v_mfma_f32_16x16x32_f16 v[98:101], v[98:101], v[188:191], v[110:113]
	s_add_u32 s34, s38, s34
	s_addc_u32 s35, s39, s35
	s_lshl_b32 s1, s48, 2
	v_mov_b32_e32 v110, v131
	v_mov_b32_e32 v111, v131
	ds_read_b64_tr_b16 v[112:113], v167 offset:37024
	v_cvt_pk_f16_f32 v90, v90, v91
	v_mfma_f32_16x16x32_f16 v[108:111], v[108:111], v[188:191], v[118:121]
	v_cvt_pk_f16_f32 v91, v92, v93
	s_nop 1
	ds_read_b64_tr_b16 v[120:121], v167 offset:37088
	v_mov_b32_e32 v118, v131
	s_waitcnt lgkmcnt(1)
	v_mfma_f32_16x16x32_f16 v[112:115], v[112:115], v[188:191], v[122:125]
	v_mov_b32_e32 v119, v131
	s_nop 1
	v_mov_b32_e32 v122, v131
	v_mov_b32_e32 v123, v131
	v_mfma_f32_16x16x32_f16 v[116:119], v[116:119], v[188:191], v[126:129]
	s_waitcnt lgkmcnt(0)
	v_mfma_f32_16x16x32_f16 v[86:89], v[120:123], v[188:191], v[86:89]
	v_add_u32_e32 v120, s26, v82
	v_mov_b32_e32 v121, v131
	v_lshlrev_b64 v[120:121], 11, v[120:121]
	v_lshl_add_u64 v[120:121], s[34:35], 0, v[120:121]
	s_and_b32 s26, s1, 0x700
	v_lshl_add_u64 v[120:121], v[120:121], 0, s[26:27]
	v_lshlrev_b32_e32 v122, 1, v132
	v_lshl_add_u64 v[120:121], v[120:121], 0, v[122:123]
	global_store_dwordx2 v[120:121], v[90:91], off
	v_cvt_pk_f16_f32 v90, v94, v95
	v_cvt_pk_f16_f32 v91, v96, v97
	global_store_dwordx2 v[120:121], v[90:91], off offset:32
	v_cvt_pk_f16_f32 v90, v98, v99
	v_cvt_pk_f16_f32 v91, v100, v101
	global_store_dwordx2 v[120:121], v[90:91], off offset:64
	v_cvt_pk_f16_f32 v90, v102, v103
	v_cvt_pk_f16_f32 v91, v104, v105
	global_store_dwordx2 v[120:121], v[90:91], off offset:96
	v_cvt_pk_f16_f32 v90, v108, v109
	v_cvt_pk_f16_f32 v91, v110, v111
	global_store_dwordx2 v[120:121], v[90:91], off offset:128
	v_cvt_pk_f16_f32 v90, v112, v113
	v_cvt_pk_f16_f32 v91, v114, v115
	global_store_dwordx2 v[120:121], v[90:91], off offset:160
	v_cvt_pk_f16_f32 v90, v116, v117
	v_cvt_pk_f16_f32 v91, v118, v119
	v_cvt_pk_f16_f32 v86, v86, v87
	v_cvt_pk_f16_f32 v87, v88, v89
	global_store_dwordx2 v[120:121], v[90:91], off offset:192
	global_store_dwordx2 v[120:121], v[86:87], off offset:224
	s_and_saveexec_b64 s[34:35], s[6:7]
	s_cbranch_execz .LBB0_476
	s_mov_b32 s1, 0x800000
	v_cmp_gt_f32_e32 vcc, s1, v106
	s_mov_b32 s26, 0x3f317217
	s_bfe_u32 s1, s48, 0x40006
	v_cndmask_b32_e64 v83, 0, 32, vcc
	v_ldexp_f32 v83, v106, v83
	v_log_f32_e32 v83, v83
	s_lshl_b32 s0, s0, 4
	s_or_b32 s0, s0, s1
	v_cndmask_b32_e32 v84, 0, v181, vcc
	v_mul_f32_e32 v86, 0x3f317217, v83
	v_fma_f32 v86, v83, s26, -v86
	v_fmac_f32_e32 v86, 0x3377d1cf, v83
	s_mov_b32 s26, 0x7f800000
	v_fmac_f32_e32 v86, 0x3f317217, v83
	v_cmp_lt_f32_e64 vcc, |v83|, s26
	s_ashr_i32 s1, s0, 31
	s_lshl_b64 s[0:1], s[0:1], 15
	v_cndmask_b32_e32 v83, v83, v86, vcc
	v_sub_f32_e32 v83, v83, v84
	s_add_u32 s0, s40, s0
	v_add_f32_e32 v84, v85, v83
	v_mov_b32_e32 v83, v131
	s_addc_u32 s1, s41, s1
	v_lshl_add_u64 v[82:83], v[82:83], 2, s[0:1]
	global_store_dword v[82:83], v84, off
	s_branch .LBB0_476

.LBB0_1044:
	s_waitcnt vmcnt(0) lgkmcnt(0)
	s_mov_b64 s[6:7], exec
	v_readfirstlane_b32 s3, v186
	s_and_b32 s14, s3, 3
	s_lshl_b32 s10, s96, 2
	s_add_i32 s14, s14, s10
	s_lshr_b32 s10, s3, 2
	s_lshl_b32 s11, s2, 2
	v_and_b32_e32 v1, 15, v0
	v_bfe_u32 v10, v0, 4, 2
	v_lshlrev_b32_e32 v11, 4, v10
	v_lshl_or_b32 v11, v1, 12, v11
	v_lshl_add_u32 v11, s10, 11, v11
	v_lshlrev_b32_e32 v25, 8, v10
	v_lshl_or_b32 v25, v1, 2, v25
	v_and_b32_e32 v24, 0xff, v0
	v_lshlrev_b32_e32 v24, 4, v24
	s_add_u32 s12, s58, 0x3d700000
	s_addc_u32 s13, s59, 0
.Lec_job:
	s_cmp_ge_u32 s14, 0x400
	s_cbranch_scc1 .Lec_done
	s_lshl_b32 s3, s14, 16
	s_add_u32 s8, s58, 0x32100000
	s_addc_u32 s9, s59, 0
	s_add_u32 s8, s8, s3
	s_addc_u32 s9, s9, 0
	s_waitcnt vmcnt(0)
	global_load_dwordx4 v[26:29], v11, s[8:9]
	global_load_dwordx4 v[100:103], v11, s[12:13]
	global_load_dwordx4 v[30:33], v11, s[8:9] offset:64
	global_load_dwordx4 v[104:107], v11, s[12:13] offset:64
	global_load_dwordx4 v[34:37], v11, s[8:9] offset:128
	global_load_dwordx4 v[108:111], v11, s[12:13] offset:128
	global_load_dwordx4 v[38:41], v11, s[8:9] offset:192
	global_load_dwordx4 v[112:115], v11, s[12:13] offset:192
	global_load_dwordx4 v[42:45], v11, s[8:9] offset:256
	global_load_dwordx4 v[116:119], v11, s[12:13] offset:256
	global_load_dwordx4 v[46:49], v11, s[8:9] offset:320
	global_load_dwordx4 v[120:123], v11, s[12:13] offset:320
	global_load_dwordx4 v[50:53], v11, s[8:9] offset:384
	global_load_dwordx4 v[124:127], v11, s[12:13] offset:384
	global_load_dwordx4 v[54:57], v11, s[8:9] offset:448
	global_load_dwordx4 v[128:131], v11, s[12:13] offset:448
	global_load_dwordx4 v[58:61], v11, s[8:9] offset:512
	global_load_dwordx4 v[132:135], v11, s[12:13] offset:512
	global_load_dwordx4 v[62:65], v11, s[8:9] offset:576
	global_load_dwordx4 v[136:139], v11, s[12:13] offset:576
	global_load_dwordx4 v[66:69], v11, s[8:9] offset:640
	global_load_dwordx4 v[140:143], v11, s[12:13] offset:640
	global_load_dwordx4 v[70:73], v11, s[8:9] offset:704
	global_load_dwordx4 v[144:147], v11, s[12:13] offset:704
	global_load_dwordx4 v[74:77], v11, s[8:9] offset:768
	global_load_dwordx4 v[148:151], v11, s[12:13] offset:768
	global_load_dwordx4 v[78:81], v11, s[8:9] offset:832
	global_load_dwordx4 v[152:155], v11, s[12:13] offset:832
	global_load_dwordx4 v[82:85], v11, s[8:9] offset:896
	global_load_dwordx4 v[156:159], v11, s[12:13] offset:896
	global_load_dwordx4 v[86:89], v11, s[8:9] offset:960
	global_load_dwordx4 v[160:163], v11, s[12:13] offset:960
	s_waitcnt vmcnt(30)
	v_mfma_f32_16x16x32_f16 v[2:5], v[26:29], v[100:103], 0
	global_load_dwordx4 v[26:29], v11, s[8:9] offset:1024
	global_load_dwordx4 v[100:103], v11, s[12:13] offset:1024
	s_waitcnt vmcnt(30)
	v_mfma_f32_16x16x32_f16 v[6:9], v[30:33], v[104:107], 0
	global_load_dwordx4 v[30:33], v11, s[8:9] offset:1088
	global_load_dwordx4 v[104:107], v11, s[12:13] offset:1088
	s_waitcnt vmcnt(30)
	v_mfma_f32_16x16x32_f16 v[2:5], v[34:37], v[108:111], v[2:5]
	global_load_dwordx4 v[34:37], v11, s[8:9] offset:1152
	global_load_dwordx4 v[108:111], v11, s[12:13] offset:1152
	s_waitcnt vmcnt(30)
	v_mfma_f32_16x16x32_f16 v[6:9], v[38:41], v[112:115], v[6:9]
	global_load_dwordx4 v[38:41], v11, s[8:9] offset:1216
	global_load_dwordx4 v[112:115], v11, s[12:13] offset:1216
	s_waitcnt vmcnt(30)
	v_mfma_f32_16x16x32_f16 v[2:5], v[42:45], v[116:119], v[2:5]
	global_load_dwordx4 v[42:45], v11, s[8:9] offset:1280
	global_load_dwordx4 v[116:119], v11, s[12:13] offset:1280
	s_waitcnt vmcnt(30)
	v_mfma_f32_16x16x32_f16 v[6:9], v[46:49], v[120:123], v[6:9]
	global_load_dwordx4 v[46:49], v11, s[8:9] offset:1344
	global_load_dwordx4 v[120:123], v11, s[12:13] offset:1344
	s_waitcnt vmcnt(30)
	v_mfma_f32_16x16x32_f16 v[2:5], v[50:53], v[124:127], v[2:5]
	global_load_dwordx4 v[50:53], v11, s[8:9] offset:1408
	global_load_dwordx4 v[124:127], v11, s[12:13] offset:1408
	s_waitcnt vmcnt(30)
	v_mfma_f32_16x16x32_f16 v[6:9], v[54:57], v[128:131], v[6:9]
	global_load_dwordx4 v[54:57], v11, s[8:9] offset:1472
	global_load_dwordx4 v[128:131], v11, s[12:13] offset:1472
	s_waitcnt vmcnt(30)
	v_mfma_f32_16x16x32_f16 v[2:5], v[58:61], v[132:135], v[2:5]
	global_load_dwordx4 v[58:61], v11, s[8:9] offset:1536
	global_load_dwordx4 v[132:135], v11, s[12:13] offset:1536
	s_waitcnt vmcnt(30)
	v_mfma_f32_16x16x32_f16 v[6:9], v[62:65], v[136:139], v[6:9]
	global_load_dwordx4 v[62:65], v11, s[8:9] offset:1600
	global_load_dwordx4 v[136:139], v11, s[12:13] offset:1600
	s_waitcnt vmcnt(30)
	v_mfma_f32_16x16x32_f16 v[2:5], v[66:69], v[140:143], v[2:5]
	global_load_dwordx4 v[66:69], v11, s[8:9] offset:1664
	global_load_dwordx4 v[140:143], v11, s[12:13] offset:1664
	s_waitcnt vmcnt(30)
	v_mfma_f32_16x16x32_f16 v[6:9], v[70:73], v[144:147], v[6:9]
	global_load_dwordx4 v[70:73], v11, s[8:9] offset:1728
	global_load_dwordx4 v[144:147], v11, s[12:13] offset:1728
	s_waitcnt vmcnt(30)
	v_mfma_f32_16x16x32_f16 v[2:5], v[74:77], v[148:151], v[2:5]
	global_load_dwordx4 v[74:77], v11, s[8:9] offset:1792
	global_load_dwordx4 v[148:151], v11, s[12:13] offset:1792
	s_waitcnt vmcnt(30)
	v_mfma_f32_16x16x32_f16 v[6:9], v[78:81], v[152:155], v[6:9]
	global_load_dwordx4 v[78:81], v11, s[8:9] offset:1856
	global_load_dwordx4 v[152:155], v11, s[12:13] offset:1856
	s_waitcnt vmcnt(30)
	v_mfma_f32_16x16x32_f16 v[2:5], v[82:85], v[156:159], v[2:5]
	global_load_dwordx4 v[82:85], v11, s[8:9] offset:1920
	global_load_dwordx4 v[156:159], v11, s[12:13] offset:1920
	s_waitcnt vmcnt(30)
	v_mfma_f32_16x16x32_f16 v[6:9], v[86:89], v[160:163], v[6:9]
	global_load_dwordx4 v[86:89], v11, s[8:9] offset:1984
	global_load_dwordx4 v[160:163], v11, s[12:13] offset:1984
	s_waitcnt vmcnt(30)
	v_mfma_f32_16x16x32_f16 v[2:5], v[26:29], v[100:103], v[2:5]
	s_waitcnt vmcnt(28)
	v_mfma_f32_16x16x32_f16 v[6:9], v[30:33], v[104:107], v[6:9]
	s_waitcnt vmcnt(26)
	v_mfma_f32_16x16x32_f16 v[2:5], v[34:37], v[108:111], v[2:5]
	s_waitcnt vmcnt(24)
	v_mfma_f32_16x16x32_f16 v[6:9], v[38:41], v[112:115], v[6:9]
	s_waitcnt vmcnt(22)
	v_mfma_f32_16x16x32_f16 v[2:5], v[42:45], v[116:119], v[2:5]
	s_waitcnt vmcnt(20)
	v_mfma_f32_16x16x32_f16 v[6:9], v[46:49], v[120:123], v[6:9]
	s_waitcnt vmcnt(18)
	v_mfma_f32_16x16x32_f16 v[2:5], v[50:53], v[124:127], v[2:5]
	s_waitcnt vmcnt(16)
	v_mfma_f32_16x16x32_f16 v[6:9], v[54:57], v[128:131], v[6:9]
	s_waitcnt vmcnt(14)
	v_mfma_f32_16x16x32_f16 v[2:5], v[58:61], v[132:135], v[2:5]
	s_waitcnt vmcnt(12)
	v_mfma_f32_16x16x32_f16 v[6:9], v[62:65], v[136:139], v[6:9]
	s_waitcnt vmcnt(10)
	v_mfma_f32_16x16x32_f16 v[2:5], v[66:69], v[140:143], v[2:5]
	s_waitcnt vmcnt(8)
	v_mfma_f32_16x16x32_f16 v[6:9], v[70:73], v[144:147], v[6:9]
	s_waitcnt vmcnt(6)
	v_mfma_f32_16x16x32_f16 v[2:5], v[74:77], v[148:151], v[2:5]
	s_waitcnt vmcnt(4)
	v_mfma_f32_16x16x32_f16 v[6:9], v[78:81], v[152:155], v[6:9]
	s_waitcnt vmcnt(2)
	v_mfma_f32_16x16x32_f16 v[2:5], v[82:85], v[156:159], v[2:5]
	s_waitcnt vmcnt(0)
	v_mfma_f32_16x16x32_f16 v[6:9], v[86:89], v[160:163], v[6:9]
	s_nop 15
	v_add_f32_e32 v2, v2, v6
	v_add_f32_e32 v3, v3, v7
	v_add_f32_e32 v4, v4, v8
	v_add_f32_e32 v5, v5, v9
	s_barrier
	s_cmp_eq_u32 s10, 0
	s_cbranch_scc1 .Lec_nowr
	ds_write_b128 v24, v[2:5]
	s_waitcnt lgkmcnt(0)
.Lec_nowr:
	s_barrier
	s_cmp_eq_u32 s10, 0
	s_cbranch_scc0 .Lec_nost
	ds_read_b128 v[6:9], v24
	s_lshl_b32 s3, s14, 10
	s_add_u32 s8, s58, 0x4c200000
	s_addc_u32 s9, s59, 0
	s_add_u32 s8, s8, s3
	s_addc_u32 s9, s9, 0
	s_waitcnt lgkmcnt(0)
	v_add_f32_e32 v2, v2, v6
	v_add_f32_e32 v3, v3, v7
	v_add_f32_e32 v4, v4, v8
	v_add_f32_e32 v5, v5, v9
	global_store_dword v25, v2, s[8:9]
	global_store_dword v25, v3, s[8:9] offset:64
	global_store_dword v25, v4, s[8:9] offset:128
	global_store_dword v25, v5, s[8:9] offset:192
.Lec_nost:
	s_add_i32 s14, s14, s11
	s_branch .Lec_job
.Lec_done:
.LBB0_1053:
	s_or_b64 exec, exec, s[6:7]
